# S5 producer: hazard pads between plain VALU ops in the recurrence steps dropped
# baseline (speedup 1.0000x reference)
; #define LAS __attribute__((address_space(3)))
; __device__ __forceinline__ unsigned cvt_pk_bf16(float lo, float hi) { unsigned r; asm volatile("v_cvt_pk_bf16_f32 %0, %1, %2" : "=v"(r) : "v"(lo), "v"(hi)); return r; }
; __device__ __forceinline__ float vfma(float a, float b, float c) { float d; asm("v_fma_f32 %0, %1, %2, %3" : "=v"(d) : "v"(a), "v"(b), "v"(c)); return d; }
; __device__ __forceinline__ float vfnma(float a, float b, float c) { float d; asm("v_fma_f32 %0, -%1, %2, %3" : "=v"(d) : "v"(a), "v"(b), "v"(c)); return d; }
; __device__ __forceinline__ void phase_s5p(const float* const (&in)[34], unsigned char* ws, LAS unsigned char* lds, int G) {
;     ...
; #pragma unroll
;                 for (int t = 0; t < 16; ++t) { const float nr = vfma(ar, xr, vfnma(ai, xi, bu[t][0])), ni = vfma(ar, xi, vfma(ai, xr, bu[t][1])); xr = nr; xi = ni;
;                     *(LAS unsigned*)(XB + t * 272 + p * 4) = cvt_pk_bf16(nr, ni);
;                     if (t & 1) accn[t >> 1] = __builtin_amdgcn_mfma_f32_16x16x32_bf16(uop, bop[t >> 1], (f32x4){0.f, 0.f, 0.f, 0.f}, 0, 0, 0);
;                     __builtin_amdgcn_sched_barrier(0); }
;                 if (ck + 1 < NCK) {
; #pragma unroll
;                     for (int nt = 0; nt < 8; ++nt) {
; #pragma unroll
;                         for (int i = 0; i < 4; ++i) BUn[(4 * fq + i) * 132 + nt * 16 + fr] = accn[nt][i]; } }
.LBB0_1484:
	s_add_i32 s4, s8, 1
	s_mulk_i32 s5, 0x1100
	v_add_u32_e32 v3, s5, v102
	s_waitcnt lgkmcnt(7)
	v_fma_f32 v4, -v95, v114, v54
	v_fma_f32 v5, v95, v94, v55
	v_fma_f32 v4, v93, v94, v4
	v_fma_f32 v5, v93, v114, v5
	v_cvt_pk_bf16_f32 v54, v4, v5
	ds_write_b32 v3, v54 offset:20992
	v_fma_f32 v54, -v95, v5, v56
	v_fma_f32 v94, v93, v4, v54
	v_fma_f32 v4, v95, v4, v57
	v_mfma_f32_16x16x32_bf16 v[54:57], v[38:41], v[10:13], 0
	v_fma_f32 v4, v93, v5, v4
	v_cvt_pk_bf16_f32 v5, v94, v4
	ds_write_b32 v3, v5 offset:21264
	s_waitcnt lgkmcnt(8)
	v_fma_f32 v5, -v95, v4, v62
	v_fma_f32 v62, v95, v94, v63
	v_fma_f32 v5, v93, v94, v5
	v_fma_f32 v4, v93, v4, v62
	v_cvt_pk_bf16_f32 v62, v5, v4
	ds_write_b32 v3, v62 offset:21536
	v_fma_f32 v62, -v95, v4, v64
	v_fma_f32 v94, v93, v5, v62
	v_fma_f32 v5, v95, v5, v65
	v_mfma_f32_16x16x32_bf16 v[62:65], v[38:41], v[6:9], 0
	v_fma_f32 v4, v93, v4, v5
	v_cvt_pk_bf16_f32 v5, v94, v4
	ds_write_b32 v3, v5 offset:21808
	s_waitcnt lgkmcnt(9)
	v_fma_f32 v5, -v95, v4, v70
	v_fma_f32 v70, v95, v94, v71
	v_fma_f32 v5, v93, v94, v5
	v_fma_f32 v4, v93, v4, v70
	v_cvt_pk_bf16_f32 v70, v5, v4
	ds_write_b32 v3, v70 offset:22080
	v_fma_f32 v70, -v95, v4, v72
	v_fma_f32 v94, v93, v5, v70
	v_fma_f32 v5, v95, v5, v73
	v_mfma_f32_16x16x32_bf16 v[70:73], v[38:41], v[18:21], 0
	v_fma_f32 v4, v93, v4, v5
	v_cvt_pk_bf16_f32 v5, v94, v4
	ds_write_b32 v3, v5 offset:22352
	s_waitcnt lgkmcnt(10)
	v_fma_f32 v5, -v95, v4, v74
	v_fma_f32 v74, v95, v94, v75
	v_fma_f32 v5, v93, v94, v5
	v_fma_f32 v4, v93, v4, v74
	v_cvt_pk_bf16_f32 v74, v5, v4
	ds_write_b32 v3, v74 offset:22624
	v_fma_f32 v74, -v95, v4, v76
	v_fma_f32 v94, v93, v5, v74
	v_fma_f32 v5, v95, v5, v77
	v_mfma_f32_16x16x32_bf16 v[74:77], v[38:41], v[14:17], 0
	v_fma_f32 v4, v93, v4, v5
	v_cvt_pk_bf16_f32 v5, v94, v4
	ds_write_b32 v3, v5 offset:22896
	s_waitcnt lgkmcnt(11)
	v_fma_f32 v5, -v95, v4, v66
	v_fma_f32 v66, v95, v94, v67
	v_fma_f32 v5, v93, v94, v5
	v_fma_f32 v4, v93, v4, v66
	v_cvt_pk_bf16_f32 v66, v5, v4
	ds_write_b32 v3, v66 offset:23168
	v_fma_f32 v66, -v95, v4, v68
	v_fma_f32 v94, v93, v5, v66
	v_fma_f32 v5, v95, v5, v69
	v_mfma_f32_16x16x32_bf16 v[66:69], v[38:41], v[26:29], 0
	v_fma_f32 v4, v93, v4, v5
	v_cvt_pk_bf16_f32 v5, v94, v4
	ds_write_b32 v3, v5 offset:23440
	s_waitcnt lgkmcnt(12)
	v_fma_f32 v5, -v95, v4, v58
	v_fma_f32 v58, v95, v94, v59
	v_fma_f32 v5, v93, v94, v5
	v_fma_f32 v4, v93, v4, v58
	v_cvt_pk_bf16_f32 v58, v5, v4
	ds_write_b32 v3, v58 offset:23712
	v_fma_f32 v58, -v95, v4, v60
	v_fma_f32 v94, v93, v5, v58
	v_fma_f32 v5, v95, v5, v61
	v_mfma_f32_16x16x32_bf16 v[58:61], v[38:41], v[22:25], 0
	v_fma_f32 v4, v93, v4, v5
	v_cvt_pk_bf16_f32 v5, v94, v4
	ds_write_b32 v3, v5 offset:23984
	s_waitcnt lgkmcnt(13)
	v_fma_f32 v5, -v95, v4, v50
	v_fma_f32 v50, v95, v94, v51
	v_fma_f32 v5, v93, v94, v5
	v_fma_f32 v4, v93, v4, v50
	v_cvt_pk_bf16_f32 v50, v5, v4
	ds_write_b32 v3, v50 offset:24256
	v_fma_f32 v50, -v95, v4, v52
	v_fma_f32 v94, v93, v5, v50
	v_fma_f32 v5, v95, v5, v53
	v_mfma_f32_16x16x32_bf16 v[50:53], v[38:41], v[34:37], 0
	v_fma_f32 v4, v93, v4, v5
	v_cvt_pk_bf16_f32 v5, v94, v4
	ds_write_b32 v3, v5 offset:24528
	s_waitcnt lgkmcnt(14)
	v_fma_f32 v5, -v95, v4, v46
	v_fma_f32 v46, v95, v94, v47
	v_fma_f32 v5, v93, v94, v5
	v_fma_f32 v4, v93, v4, v46
	v_cvt_pk_bf16_f32 v46, v5, v4
	ds_write_b32 v3, v46 offset:24800
	v_mfma_f32_16x16x32_bf16 v[38:41], v[38:41], v[30:33], 0
	v_fma_f32 v46, -v95, v4, v48
	v_fma_f32 v94, v93, v5, v46
	v_fma_f32 v5, v95, v5, v49
	v_fma_f32 v114, v93, v4, v5
	v_cvt_pk_bf16_f32 v4, v94, v114
	ds_write_b32 v3, v4 offset:25072
	s_cmpk_eq_i32 s8, 0x80
	s_cbranch_scc1 .LBB0_1478
	s_bitcmp1_b32 s4, 0
	s_cselect_b32 s5, 0x2100, 0
	v_add_u32_e32 v3, s5, v103
	v_add_u32_e32 v4, 0x1000, v3
	v_add_u32_e32 v3, 0x1400, v3
	ds_write2_b32 v4, v54, v62 offset1:16
	ds_write2_b32 v4, v55, v63 offset0:132 offset1:148
	ds_write2_b32 v3, v56, v64 offset0:8 offset1:24
	ds_write2_b32 v3, v57, v65 offset0:140 offset1:156
	ds_write2_b32 v4, v70, v74 offset0:32 offset1:48
	ds_write2_b32 v4, v71, v75 offset0:164 offset1:180
	ds_write2_b32 v3, v72, v76 offset0:40 offset1:56
	ds_write2_b32 v3, v73, v77 offset0:172 offset1:188
	ds_write2_b32 v4, v66, v58 offset0:64 offset1:80
	ds_write2_b32 v4, v67, v59 offset0:196 offset1:212
	ds_write2_b32 v3, v68, v60 offset0:72 offset1:88
	ds_write2_b32 v3, v69, v61 offset0:204 offset1:220
	ds_write2_b32 v4, v50, v38 offset0:96 offset1:112
	ds_write2_b32 v4, v51, v39 offset0:228 offset1:244
	ds_write2_b32 v3, v52, v40 offset0:104 offset1:120
	ds_write2_b32 v3, v53, v41 offset0:236 offset1:252
	s_branch .LBB0_1478
